# sel PV: P split in two 32-key halves, second-half exps and the row-sum adds interleaved between the PV MFMAs (same accumulate order)
# speedup vs baseline: 1.0144x; 1.0076x over previous
; __device__ __forceinline__ unsigned pk4_fp8(float a, float b, float c, float d) { unsigned w = 0u; w = __builtin_amdgcn_cvt_pk_fp8_f32(a, b, w, false); w = __builtin_amdgcn_cvt_pk_fp8_f32(c, d, w, true); return w; }
; #define LGKM_W(n) asm volatile("s_waitcnt lgkmcnt(" #n ")" ::: "memory"); SBAR()
; #define PV8_MM(dt) do { g.o[dt] = __builtin_amdgcn_mfma_f32_16x16x32_fp8_fp8(f.a[dt][0], b0, g.o[dt], 0, 0, 0); g.o[dt] = __builtin_amdgcn_mfma_f32_16x16x32_fp8_fp8(f.a[dt][1], b1, g.o[dt], 0, 0, 0); } while (0)
; template <class G> __device__ __forceinline__ void pv8_mm(G& g, const f32x4 (&s)[4], const VT8Frag& f) {
;     ...
;     unsigned pa[4];
; #pragma unroll
;     for (int T_ = 0; T_ < 4; ++T_) pa[T_] = pk4_fp8(s[T_][0], s[T_][1], s[T_][2], s[T_][3]);
;     const long b0 = (long)(((unsigned long long)pa[1] << 32) | pa[0]), b1 = (long)(((unsigned long long)pa[3] << 32) | pa[2]);
;     LGKM_W(14); PV8_MM(0); LGKM_W(12); PV8_MM(1); LGKM_W(10); PV8_MM(2); LGKM_W(8); PV8_MM(3);
;     LGKM_W(6); PV8_MM(4); LGKM_W(4); PV8_MM(5); LGKM_W(2); PV8_MM(6); LGKM_W(0); PV8_MM(7);
; template <class G> __device__ __forceinline__ void online_sm8(f32x4 (&s)[4], G& g, const float ref) {
;     ...
;     float ps = 0.f;
; #pragma unroll
;     for (int T_ = 0; T_ < 4; ++T_)
; #pragma unroll
;         for (int i = 0; i < 4; ++i) { s[T_][i] = __builtin_amdgcn_exp2f(s[T_][i]); ps += s[T_][i]; }
;     g.l += ps;
.LBB0_1797:
	v_exp_f32_e32 v240, v84
	v_exp_f32_e32 v241, v85
	v_exp_f32_e32 v242, v86
	v_exp_f32_e32 v243, v87
	v_exp_f32_e32 v244, v88
	v_exp_f32_e32 v245, v89
	v_exp_f32_e32 v246, v90
	v_exp_f32_e32 v247, v91
	s_waitcnt lgkmcnt(0)
	v_cvt_pk_fp8_f32 v84, v240, v241
	v_cvt_pk_fp8_f32 v85, v244, v245
	v_cvt_pk_fp8_f32 v84, v242, v243 op_sel:[0,0,1]
	v_cvt_pk_fp8_f32 v85, v246, v247 op_sel:[0,0,1]
	v_exp_f32_e32 v248, v92
	v_exp_f32_e32 v249, v93
	v_mfma_f32_16x16x32_fp8_fp8 v[48:51], v[148:149], v[84:85], v[48:51]
	v_exp_f32_e32 v250, v94
	v_mfma_f32_16x16x32_fp8_fp8 v[44:47], v[144:145], v[84:85], v[44:47]
	v_exp_f32_e32 v251, v95
	v_mfma_f32_16x16x32_fp8_fp8 v[40:43], v[140:141], v[84:85], v[40:43]
	v_exp_f32_e32 v252, v96
	v_mfma_f32_16x16x32_fp8_fp8 v[36:39], v[138:139], v[84:85], v[36:39]
	v_exp_f32_e32 v253, v97
	v_mfma_f32_16x16x32_fp8_fp8 v[32:35], v[132:133], v[84:85], v[32:35]
	v_exp_f32_e32 v254, v98
	v_mfma_f32_16x16x32_fp8_fp8 v[28:31], v[128:129], v[84:85], v[28:31]
	v_exp_f32_e32 v255, v99
	v_mfma_f32_16x16x32_fp8_fp8 v[24:27], v[124:125], v[84:85], v[24:27]
	v_mfma_f32_16x16x32_fp8_fp8 v[20:23], v[118:119], v[84:85], v[20:23]
	v_cvt_pk_fp8_f32 v86, v248, v249
	v_cvt_pk_fp8_f32 v87, v252, v253
	v_cvt_pk_fp8_f32 v86, v250, v251 op_sel:[0,0,1]
	v_cvt_pk_fp8_f32 v87, v254, v255 op_sel:[0,0,1]
	v_add_f32_e32 v240, v240, v241
	v_add_f32_e32 v242, v242, v243
	v_mfma_f32_16x16x32_fp8_fp8 v[48:51], v[146:147], v[86:87], v[48:51]
	v_add_f32_e32 v244, v244, v245
	v_add_f32_e32 v246, v246, v247
	v_mfma_f32_16x16x32_fp8_fp8 v[44:47], v[142:143], v[86:87], v[44:47]
	v_add_f32_e32 v248, v248, v249
	v_add_f32_e32 v250, v250, v251
	v_mfma_f32_16x16x32_fp8_fp8 v[40:43], v[136:137], v[86:87], v[40:43]
	v_add_f32_e32 v252, v252, v253
	v_add_f32_e32 v254, v254, v255
	v_mfma_f32_16x16x32_fp8_fp8 v[36:39], v[134:135], v[86:87], v[36:39]
	v_add_f32_e32 v240, v240, v242
	v_add_f32_e32 v244, v244, v246
	v_mfma_f32_16x16x32_fp8_fp8 v[32:35], v[130:131], v[86:87], v[32:35]
	v_add_f32_e32 v248, v248, v250
	v_add_f32_e32 v252, v252, v254
	v_mfma_f32_16x16x32_fp8_fp8 v[28:31], v[126:127], v[86:87], v[28:31]
	v_add_f32_e32 v240, v240, v244
	v_add_f32_e32 v248, v248, v252
	v_mfma_f32_16x16x32_fp8_fp8 v[24:27], v[120:121], v[86:87], v[24:27]
	v_add_f32_e32 v240, v240, v248
	v_add_f32_e32 v182, v182, v240
	v_mfma_f32_16x16x32_fp8_fp8 v[20:23], v[122:123], v[86:87], v[20:23]

; __device__ __forceinline__ unsigned pk4_fp8(float a, float b, float c, float d) { unsigned w = 0u; w = __builtin_amdgcn_cvt_pk_fp8_f32(a, b, w, false); w = __builtin_amdgcn_cvt_pk_fp8_f32(c, d, w, true); return w; }
; #define LGKM_W(n) asm volatile("s_waitcnt lgkmcnt(" #n ")" ::: "memory"); SBAR()
; #define PV8_MM(dt) do { g.o[dt] = __builtin_amdgcn_mfma_f32_16x16x32_fp8_fp8(f.a[dt][0], b0, g.o[dt], 0, 0, 0); g.o[dt] = __builtin_amdgcn_mfma_f32_16x16x32_fp8_fp8(f.a[dt][1], b1, g.o[dt], 0, 0, 0); } while (0)
; template <class G> __device__ __forceinline__ void pv8_mm(G& g, const f32x4 (&s)[4], const VT8Frag& f) {
;     ...
;     unsigned pa[4];
; #pragma unroll
;     for (int T_ = 0; T_ < 4; ++T_) pa[T_] = pk4_fp8(s[T_][0], s[T_][1], s[T_][2], s[T_][3]);
;     const long b0 = (long)(((unsigned long long)pa[1] << 32) | pa[0]), b1 = (long)(((unsigned long long)pa[3] << 32) | pa[2]);
;     LGKM_W(14); PV8_MM(0); LGKM_W(12); PV8_MM(1); LGKM_W(10); PV8_MM(2); LGKM_W(8); PV8_MM(3);
;     LGKM_W(6); PV8_MM(4); LGKM_W(4); PV8_MM(5); LGKM_W(2); PV8_MM(6); LGKM_W(0); PV8_MM(7);
;     ...
; }
; template <class G> __device__ __forceinline__ void online_sm8(f32x4 (&s)[4], G& g, const float ref) {
;     ...
;     float ps = 0.f;
; #pragma unroll
;     for (int T_ = 0; T_ < 4; ++T_)
; #pragma unroll
;         for (int i = 0; i < 4; ++i) { s[T_][i] = __builtin_amdgcn_exp2f(s[T_][i]); ps += s[T_][i]; }
;     g.l += ps;
.LBB0_1808:
	v_exp_f32_e32 v240, v84
	v_exp_f32_e32 v241, v85
	v_exp_f32_e32 v242, v86
	v_exp_f32_e32 v243, v87
	v_exp_f32_e32 v244, v88
	v_exp_f32_e32 v245, v89
	v_exp_f32_e32 v246, v90
	v_exp_f32_e32 v247, v91
	s_waitcnt lgkmcnt(0)
	v_cvt_pk_fp8_f32 v84, v240, v241
	v_cvt_pk_fp8_f32 v85, v244, v245
	v_cvt_pk_fp8_f32 v84, v242, v243 op_sel:[0,0,1]
	v_cvt_pk_fp8_f32 v85, v246, v247 op_sel:[0,0,1]
	v_exp_f32_e32 v248, v92
	v_exp_f32_e32 v249, v93
	v_mfma_f32_16x16x32_fp8_fp8 v[80:83], v[148:149], v[84:85], v[80:83]
	v_exp_f32_e32 v250, v94
	v_mfma_f32_16x16x32_fp8_fp8 v[76:79], v[144:145], v[84:85], v[76:79]
	v_exp_f32_e32 v251, v95
	v_mfma_f32_16x16x32_fp8_fp8 v[72:75], v[140:141], v[84:85], v[72:75]
	v_exp_f32_e32 v252, v96
	v_mfma_f32_16x16x32_fp8_fp8 v[68:71], v[138:139], v[84:85], v[68:71]
	v_exp_f32_e32 v253, v97
	v_mfma_f32_16x16x32_fp8_fp8 v[64:67], v[132:133], v[84:85], v[64:67]
	v_exp_f32_e32 v254, v98
	v_mfma_f32_16x16x32_fp8_fp8 v[60:63], v[128:129], v[84:85], v[60:63]
	v_exp_f32_e32 v255, v99
	v_mfma_f32_16x16x32_fp8_fp8 v[56:59], v[124:125], v[84:85], v[56:59]
	v_mfma_f32_16x16x32_fp8_fp8 v[52:55], v[118:119], v[84:85], v[52:55]
	v_cvt_pk_fp8_f32 v86, v248, v249
	v_cvt_pk_fp8_f32 v87, v252, v253
	v_cvt_pk_fp8_f32 v86, v250, v251 op_sel:[0,0,1]
	v_cvt_pk_fp8_f32 v87, v254, v255 op_sel:[0,0,1]
	v_add_f32_e32 v240, v240, v241
	v_add_f32_e32 v242, v242, v243
	v_mfma_f32_16x16x32_fp8_fp8 v[80:83], v[146:147], v[86:87], v[80:83]
	v_add_f32_e32 v244, v244, v245
	v_add_f32_e32 v246, v246, v247
	v_mfma_f32_16x16x32_fp8_fp8 v[76:79], v[142:143], v[86:87], v[76:79]
	v_add_f32_e32 v248, v248, v249
	v_add_f32_e32 v250, v250, v251
	v_mfma_f32_16x16x32_fp8_fp8 v[72:75], v[136:137], v[86:87], v[72:75]
	v_add_f32_e32 v252, v252, v253
	v_add_f32_e32 v254, v254, v255
	v_mfma_f32_16x16x32_fp8_fp8 v[68:71], v[134:135], v[86:87], v[68:71]
	v_add_f32_e32 v240, v240, v242
	v_add_f32_e32 v244, v244, v246
	v_mfma_f32_16x16x32_fp8_fp8 v[64:67], v[130:131], v[86:87], v[64:67]
	v_add_f32_e32 v248, v248, v250
	v_add_f32_e32 v252, v252, v254
	v_mfma_f32_16x16x32_fp8_fp8 v[60:63], v[126:127], v[86:87], v[60:63]
	v_add_f32_e32 v240, v240, v244
	v_add_f32_e32 v248, v248, v252
	v_mfma_f32_16x16x32_fp8_fp8 v[56:59], v[120:121], v[86:87], v[56:59]
	v_add_f32_e32 v240, v240, v248
	v_add_f32_e32 v183, v183, v240
	v_mfma_f32_16x16x32_fp8_fp8 v[52:55], v[122:123], v[86:87], v[52:55]
